# code placement: one 4-byte pad behind P1 puts the dense-attention loop and every GEMM K-loop back on the baseline's byte phase (mod 8)
# speedup vs baseline: 1.0153x; 1.0153x over previous
; __device__ __forceinline__ unsigned xb_ld(unsigned* p)              { return __hip_atomic_load(p, __ATOMIC_RELAXED, __HIP_MEMORY_SCOPE_AGENT); }
; __device__ __forceinline__ unsigned xb_add(unsigned* p, unsigned v) { return __hip_atomic_fetch_add(p, v, __ATOMIC_RELAXED, __HIP_MEMORY_SCOPE_AGENT); }
; __device__ __forceinline__ void xcd_barrier_complete(unsigned* bar, unsigned x, unsigned& nloc, unsigned& nx) {
;     const unsigned G = gridDim.x * gridDim.y * gridDim.z;
;     unsigned sum, cnt, mine, sp = 0u;
;     for (;;) {
;         sum = 0u; cnt = 0u; mine = 0u;
; #pragma unroll
;         for (unsigned j = 0; j < 16; ++j) { const unsigned c = xb_ld(&bar[XB_XCNT(j)]); sum += c; cnt += (c > 0u) ? 1u : 0u; mine = (j == x) ? c : mine; }
;         if (sum == G) break;
;         __builtin_amdgcn_s_sleep(1);
;         if ((++sp & 255u) == 0u) { if (xb_ld(&bar[XB_TMO])) break; if (sp > XB_SPIN_CAP) { atomicAdd(&bar[XB_TMO], 1u); break; } }
;     }
;     nloc = mine > 0u ? mine : 1u; nx = cnt > 0u ? cnt : 1u;
; }
; __device__ __forceinline__ void xcd_barrier_arrive(const XcdBarrier& b) {
;     asm volatile("s_waitcnt vmcnt(0)" ::: "memory");
;     __syncthreads();
;     if (threadIdx.x == 0) {
;         unsigned* bar = b.bar;
;         __builtin_amdgcn_s_waitcnt(0);
;         unsigned nloc = b.st[0], nx = b.st[1];
;         if (nloc == 0u) { xcd_barrier_complete(bar, b.x, nloc, nx); b.st[0] = nloc; b.st[1] = nx; }
;         const unsigned old = xb_add(&bar[XB_XSUB(b.x)], 1u);
.LBB0_284:
	s_nop 0
	v_readlane_b32 s0, v254, 12
	v_readlane_b32 s1, v254, 13
	s_cmp_gt_u32 s1, 2
	s_cselect_b64 s[0:1], -1, 0
	s_and_b64 s[0:1], s[20:21], s[0:1]
	s_andn2_b64 vcc, exec, s[0:1]
	s_mov_b32 s86, s90
	s_mov_b32 s87, s91
	s_cbranch_vccnz .LBB0_321
	s_waitcnt vmcnt(0)
	s_waitcnt vmcnt(0) lgkmcnt(0)
	s_barrier
	s_mov_b64 s[2:3], exec
	v_readlane_b32 s0, v254, 49
	v_readlane_b32 s1, v254, 50
	s_and_b64 s[0:1], s[2:3], s[0:1]
	s_mov_b64 exec, s[0:1]
	s_cbranch_execz .LBB0_320
	s_add_i32 s0, 0, 0x24160
	v_mov_b32_e32 v1, s0
	s_waitcnt vmcnt(0) expcnt(0) lgkmcnt(0)
	ds_read_b32 v2, v1
	s_add_i32 s0, 0, 0x24164
	v_mov_b32_e32 v1, s0
	ds_read_b32 v1, v1
	s_waitcnt lgkmcnt(1)
	v_cmp_ne_u32_e32 vcc, 0, v2
	s_cbranch_vccnz .LBB0_301
	v_readlane_b32 s4, v254, 7
	v_readlane_b32 s5, v254, 8
	s_load_dwordx2 s[0:1], s[4:5], 0x4
	v_readlane_b32 s18, v254, 0
	v_readlane_b32 s19, v254, 1
	s_add_u32 s4, s18, 0x4200
	s_addc_u32 s5, s19, 0
	s_add_u32 s6, s18, 0x4400
	s_addc_u32 s7, s19, 0
	v_readlane_b32 s8, v254, 9
	s_waitcnt lgkmcnt(0)
	s_mul_i32 s0, s0, s8
	s_add_u32 s8, s18, 0x4500
	s_addc_u32 s9, s19, 0
	s_add_u32 s10, s18, 0x4600
	s_addc_u32 s11, s19, 0
	s_add_u32 s14, s18, 0x4700
	s_addc_u32 s15, s19, 0
	s_add_u32 s16, s18, 0x4800
	s_addc_u32 s17, s19, 0
	s_add_u32 s20, s18, 0x4900
	s_addc_u32 s21, s19, 0
	s_add_u32 s22, s18, 0x4a00
	s_addc_u32 s23, s19, 0
	s_add_u32 s24, s18, 0x4b00
	s_addc_u32 s25, s19, 0
	s_add_u32 s26, s18, 0x4c00
	s_addc_u32 s27, s19, 0
	s_add_u32 s28, s18, 0x4d00
	s_addc_u32 s29, s19, 0
	s_add_u32 s30, s18, 0x4e00
	s_addc_u32 s31, s19, 0
	s_add_u32 s34, s18, 0x4f00
	s_addc_u32 s35, s19, 0
	s_add_u32 s36, s18, 0x5000
	s_addc_u32 s37, s19, 0
	s_add_u32 s38, s18, 0x5100
	s_addc_u32 s39, s19, 0
	s_add_u32 s40, s18, 0x5200
	s_addc_u32 s41, s19, 0
	s_add_u32 s42, s18, 0x5300
	s_mul_i32 s0, s0, s1
	s_addc_u32 s43, s19, 0
	s_mov_b32 s1, 1
	v_mov_b32_e32 v17, 0
	s_branch .LBB0_289
